# tie-candidate prefetch loop: threshold entry read as one b96 together with the tie-mask read, candidates enumerated by the branch-free 64-bit lowest-bit loop; on top of v23
# speedup vs baseline: 1.0078x; 1.0078x over previous
.LBB0_566:
	v_readlane_b32 s0, v251, 50
	s_add_i32 s40, s35, s0
	s_lshl_b32 s0, s40, 4
	s_add_i32 s0, s0, 0
	s_add_i32 s1, s0, 0x23000
	v_mov_b32_e32 v0, s1
	s_waitcnt vmcnt(2)
	ds_read_b96 v[8:10], v0
	s_lshl_b32 s41, s40, 9
	v_add_u32_e32 v0, s41, v6
	ds_read_b64 v[4:5], v0 offset:32768
	s_waitcnt lgkmcnt(1)
	v_mov_b32_e32 v2, v9
	v_mov_b32_e32 v3, v10
	v_cmp_gt_i32_e32 vcc, 1, v2
	s_cbranch_vccnz .LBB0_565
	s_movk_i32 s0, 0x80
	v_cmp_ge_i32_e32 vcc, v2, v3
	v_cmp_eq_u32_e64 s[0:1], s0, v8
	s_or_b64 s[0:1], vcc, s[0:1]
	v_cmp_lt_i32_e32 vcc, 64, v3
	s_or_b64 s[0:1], vcc, s[0:1]
	s_and_b64 vcc, exec, s[0:1]
	s_cbranch_vccnz .LBB0_565
	s_waitcnt lgkmcnt(0)
	v_bcnt_u32_b32 v0, v4, 0
	v_bcnt_u32_b32 v0, v5, v0
	v_mov_b32_e32 v11, v0
	s_nop 1
	v_add_u32_dpp v11, v11, v11 row_shr:1 row_mask:0xf bank_mask:0xf
	s_nop 1
	v_add_u32_dpp v11, v11, v11 row_shr:2 row_mask:0xf bank_mask:0xf
	s_nop 1
	v_add_u32_dpp v11, v11, v11 row_shr:4 row_mask:0xf bank_mask:0xf
	s_nop 1
	v_add_u32_dpp v11, v11, v11 row_shr:8 row_mask:0xf bank_mask:0xf
	s_nop 1
	v_add_u32_dpp v11, v11, v11 row_bcast:15 row_mask:0xa bank_mask:0xf
	s_nop 1
	v_add_u32_dpp v11, v11, v11 row_bcast:31 row_mask:0xc bank_mask:0xf
	v_sub_u32_e32 v12, v11, v0
	v_sub_u32_e32 v13, 64, v12
	v_min_i32_e32 v0, v0, v13
	v_lshl_add_u32 v2, v12, 1, s34
.Lcand_w_a:
	v_cmpx_lt_i32_e32 vcc, 0, v0
	v_ffbl_b32_e32 v8, v4
	v_ffbl_b32_e32 v9, v5
	v_or_b32_e32 v9, 32, v9
	v_min_u32_e32 v8, v8, v9
	v_or_b32_e32 v8, v8, v7
	ds_write_b16 v2, v8
	v_add_co_u32_e32 v10, vcc, -1, v4
	v_addc_co_u32_e32 v13, vcc, -1, v5, vcc
	v_and_b32_e32 v4, v4, v10
	v_and_b32_e32 v5, v5, v13
	v_add_u32_e32 v2, 2, v2
	v_add_u32_e32 v0, -1, v0
	s_cbranch_execnz .Lcand_w_a
	s_mov_b64 exec, -1
	s_mov_b64 s[0:1], -1
